# baseline (speedup 1.0000x reference)
_ZN12_GLOBAL__N_113search_kernelEPKfS1_PhPf:
	s_load_dwordx2 s[8:9], s[0:1], 0x0
	s_load_dwordx2 s[4:5], s[0:1], 0x10
	s_movk_i32 s3, 0x90
	v_readfirstlane_b32 s10, v0
	v_cmp_gt_u32_e32 vcc, s3, v0
	s_and_saveexec_b64 s[6:7], vcc
	v_mov_b32_e32 v2, -1
	v_lshlrev_b32_e32 v1, 3, v0
	v_mov_b32_e32 v3, v2
	ds_write_b64 v1, v[2:3] offset:16384
	s_or_b64 exec, exec, s[6:7]
	s_waitcnt lgkmcnt(0)
	s_add_u32 s6, s4, 0x240000
	s_addc_u32 s7, s5, 0
	s_lshl_b32 s11, s2, 1
	s_and_b32 s14, s11, 14
	s_ashr_i32 s11, s2, 7
	s_lshr_b32 s15, s10, 6
	s_add_i32 s14, s14, s11
	s_bfe_u32 s2, s2, 0x40003
	s_mul_i32 s11, s15, 24
	v_mul_u32_u24_e32 v2, 0x71d, v0
	v_mul_u32_u24_e32 v4, 0x195, v0
	s_min_u32 s18, s11, 0xa5
	s_mul_i32 s11, s14, 3
	s_mul_i32 s12, s2, 9
	s_mov_b32 s13, 0
	v_lshrrev_b32_e32 v3, 16, v2
	s_movk_i32 s19, 0xffdc
	v_lshrrev_b32_e32 v5, 17, v4
	v_mad_i32_i24 v2, v3, s19, v0
	v_mad_i32_i24 v4, v5, -9, v3
	v_add_u32_e32 v3, s11, v5
	v_mov_b64_e32 v[6:7], s[12:13]
	v_mad_i64_i32 v[8:9], s[16:17], v3, s3, v[6:7]
	v_ashrrev_i32_e32 v5, 31, v4
	v_lshl_add_u64 v[4:5], v[8:9], 0, v[4:5]
	s_movk_i32 s13, 0x240
	v_mov_b64_e32 v[8:9], s[8:9]
	v_mad_u64_u32 v[10:11], s[8:9], v4, s13, v[8:9]
	v_min_u32_e32 v4, 0x1cb, v0
	v_or_b32_e32 v4, 0x200, v4
	v_mad_i32_i24 v11, v5, s13, v11
	v_mul_u32_u24_e32 v5, 0x71d, v4
	v_ashrrev_i32_e32 v3, 31, v2
	v_lshrrev_b32_e32 v5, 16, v5
	v_lshl_add_u64 v[2:3], v[2:3], 4, v[10:11]
	v_mad_i32_i24 v10, v5, s19, v4
	v_mul_u32_u24_e32 v4, 0x653, v4
	v_lshrrev_b32_e32 v11, 19, v4
	v_mad_i32_i24 v4, v11, -9, v5
	v_add_u32_e32 v5, s11, v11
	v_mad_i64_i32 v[6:7], s[8:9], v5, s3, v[6:7]
	v_ashrrev_i32_e32 v5, 31, v4
	v_lshl_add_u64 v[4:5], v[6:7], 0, v[4:5]
	v_mad_u64_u32 v[12:13], s[8:9], v4, s13, v[8:9]
	s_mul_i32 s8, s14, 0x90
	s_barrier
	s_load_dwordx2 s[42:43], s[0:1], 0x8
	s_load_dwordx2 s[62:63], s[0:1], 0x0
	v_mov_b32_e32 v244, v2
	v_mov_b32_e32 v245, v3
	global_load_dwordx4 v[6:9], v[2:3], off
	v_mad_i32_i24 v13, v5, s13, v13
	v_ashrrev_i32_e32 v11, 31, v10
	v_lshl_add_u64 v[10:11], v[10:11], 4, v[12:13]
	v_mov_b32_e32 v246, v10
	v_mov_b32_e32 v247, v11
	global_load_dwordx4 v[10:13], v[10:11], off
	v_and_b32_e32 v1, 63, v0
	s_add_i32 s20, s8, s12
	s_lshl_b32 s20, s20, 10
	v_lshl_add_u32 v164, v1, 4, s20
	s_mul_i32 s9, s14, 0xbd
	s_add_i32 s21, s9, s18
	s_lshl_b32 s21, s21, 10
	v_lshl_add_u32 v165, v1, 4, s21
	s_add_u32 s22, s4, 0x1000
	s_addc_u32 s23, s5, 0
	s_add_u32 s24, s4, 0x2000
	s_addc_u32 s25, s5, 0
	s_mov_b32 s26, s6
	s_mov_b32 s27, s7
	s_add_u32 s28, s6, 0x1000
	s_addc_u32 s29, s7, 0
	s_add_u32 s30, s6, 0x2000
	s_addc_u32 s31, s7, 0
	s_add_u32 s32, s6, 0x3000
	s_addc_u32 s33, s7, 0
	s_add_u32 s34, s6, 0x4000
	s_addc_u32 s35, s7, 0
	s_add_u32 s36, s6, 0x5000
	s_addc_u32 s37, s7, 0
	v_bfe_u32 v166, v0, 4, 2
	v_and_b32_e32 v167, 15, v0
	v_lshlrev_b32_e32 v167, 3, v167
	s_mul_i32 s40, s15, 6
	s_mov_b32 s41, 0x7f000000
	global_load_dwordx4 v[112:115], v164, s[4:5]
	global_load_dwordx4 v[16:19], v165, s[26:27] nt
	global_load_dwordx4 v[20:23], v165, s[26:27] offset:1024 nt
	global_load_dwordx4 v[24:27], v165, s[26:27] offset:2048 nt
	global_load_dwordx4 v[28:31], v165, s[26:27] offset:3072 nt
	global_load_dwordx4 v[32:35], v165, s[28:29] nt
	global_load_dwordx4 v[36:39], v165, s[28:29] offset:1024 nt
	global_load_dwordx4 v[40:43], v165, s[28:29] offset:2048 nt
	global_load_dwordx4 v[44:47], v165, s[28:29] offset:3072 nt
	global_load_dwordx4 v[48:51], v165, s[30:31] nt
	global_load_dwordx4 v[52:55], v165, s[30:31] offset:1024 nt
	global_load_dwordx4 v[56:59], v165, s[30:31] offset:2048 nt
	global_load_dwordx4 v[60:63], v165, s[30:31] offset:3072 nt
	global_load_dwordx4 v[64:67], v165, s[32:33] nt
	global_load_dwordx4 v[68:71], v165, s[32:33] offset:1024 nt
	global_load_dwordx4 v[72:75], v165, s[32:33] offset:2048 nt
	global_load_dwordx4 v[76:79], v165, s[32:33] offset:3072 nt
	global_load_dwordx4 v[80:83], v165, s[34:35] nt
	global_load_dwordx4 v[84:87], v165, s[34:35] offset:1024 nt
	global_load_dwordx4 v[88:91], v165, s[34:35] offset:2048 nt
	global_load_dwordx4 v[92:95], v165, s[34:35] offset:3072 nt
	global_load_dwordx4 v[96:99], v165, s[36:37] nt
	global_load_dwordx4 v[100:103], v165, s[36:37] offset:1024 nt
	global_load_dwordx4 v[104:107], v165, s[36:37] offset:2048 nt
	global_load_dwordx4 v[108:111], v165, s[36:37] offset:3072 nt
	global_load_dwordx4 v[116:119], v164, s[4:5] offset:1024
	v_lshlrev_b32_e32 v14, 4, v0
	s_lshr_b32 s50, s15, 1
	s_and_b32 s51, s15, 1
	s_lshl_b32 s51, s51, 3
	s_mov_b32 s48, 0x1010101
	s_mov_b32 s49, 0x1010101
	s_movk_i32 s58, 0x900
	s_movk_i32 s59, 0xb40
	v_and_b32_e32 v168, 7, v0
	v_lshrrev_b32_e32 v177, 3, v1
	v_or_b32_e32 v177, s51, v177
	v_lshlrev_b32_e32 v169, 3, v177
	v_and_b32_e32 v179, 3, v0
	v_lshlrev_b32_e32 v179, 8, v179
	v_lshl_add_u32 v170, v177, 4, v179
	v_add_u32_e32 v170, s20, v170
	v_lshrrev_b32_e32 v179, 2, v168
	v_and_b32_e32 v180, 3, v0
	v_lshl_or_b32 v171, v179, 4, v180
	v_mul_u32_u24_e32 v179, 11, v168
	v_lshrrev_b32_e32 v179, 5, v179
	v_mul_u32_u24_e32 v180, 3, v179
	v_sub_u32_e32 v180, v168, v180
	v_mul_u32_u24_e32 v181, 0x90, v179
	v_add_u32_e32 v181, v181, v180
	v_mul_u32_u24_e32 v172, 0x240, v181
	v_mul_u32_u24_e32 v181, 0x48, v179
	v_add_u32_e32 v181, v181, v180
	v_mul_u32_u24_e32 v173, 0x120, v181
	v_mul_u32_u24_e32 v181, 0x24, v179
	v_add_u32_e32 v181, v181, v180
	v_mul_u32_u24_e32 v174, 0x90, v181
	v_mul_u32_u24_e32 v181, 9, v179
	v_add_u32_e32 v181, v181, v180
	v_mul_u32_u24_e32 v175, 0x240, v181
	v_add_u32_e32 v176, 8, v168
	s_waitcnt lgkmcnt(0)
	s_mul_i32 s60, s14, 0x3cc00
	s_add_u32 s42, s42, s60
	s_addc_u32 s43, s43, 0
	s_mul_i32 s60, s14, 0xf300
	s_add_u32 s44, s4, s60
	s_addc_u32 s45, s5, 0
	s_add_u32 s44, s44, 0x534000
	s_addc_u32 s45, s45, 0
	s_mul_i32 s60, s14, 0x3cc0
	s_add_u32 s46, s4, s60
	s_addc_u32 s47, s5, 0
	s_add_u32 s46, s46, 0x627000
	s_addc_u32 s47, s47, 0
	v_mov_b32_e32 v152, s42
	v_mov_b32_e32 v153, s43
	v_mov_b32_e32 v154, s44
	v_mov_b32_e32 v155, s45
	v_mov_b32_e32 v159, s46
	v_mov_b32_e32 v161, s47
	s_sub_u32 s60, s42, s62
	s_subb_u32 s61, s43, s63
	s_mul_i32 s62, s14, 0x3cc00
	s_sub_u32 s60, s60, s62
	s_subb_u32 s61, s61, 0
	v_lshl_add_u64 v[244:245], v[244:245], 0, s[60:61]
	v_lshl_add_u64 v[246:247], v[246:247], 0, s[60:61]
	s_lshl_b32 s62, s15, 10
	s_add_i32 s62, s62, 0x46e0
	s_mov_b32 m0, s62
	s_mul_i32 s62, s2, 0xf30
	s_add_u32 s60, s44, s62
	s_addc_u32 s61, s45, 0
	v_lshlrev_b32_e32 v240, 4, v0
	v_mov_b32_e32 v241, 0
	v_lshl_add_u64 v[240:241], v[240:241], 0, s[60:61]
	s_mul_i32 s62, s2, 0x3cc
	s_add_u32 s60, s46, s62
	s_addc_u32 s61, s47, 0
	v_lshlrev_b32_e32 v242, 2, v0
	v_mov_b32_e32 v243, 0
	v_lshl_add_u64 v[242:243], v[242:243], 0, s[60:61]
	global_load_lds_dwordx4 v[244:245], off
	global_load_lds_dwordx4 v[246:247], off
	global_load_lds_dwordx4 v[240:241], off
	global_load_lds_dword v[242:243], off
	s_load_dwordx2 s[2:3], s[0:1], 0x18
	s_waitcnt vmcnt(25)
	ds_write_b128 v14, v[6:9]
	ds_write_b128 v14, v[10:13] offset:8192
	v_mfma_f32_16x16x32_f16 v[120:123], v[16:19], v[112:115], 0
	v_mfma_f32_16x16x32_f16 v[124:127], v[20:23], v[112:115], 0
	v_mfma_f32_16x16x32_f16 v[128:131], v[24:27], v[112:115], 0
	v_mfma_f32_16x16x32_f16 v[132:135], v[28:31], v[112:115], 0
	s_waitcnt vmcnt(21)
	v_mfma_f32_16x16x32_f16 v[136:139], v[32:35], v[112:115], 0
	v_mfma_f32_16x16x32_f16 v[140:143], v[36:39], v[112:115], 0
	v_mfma_f32_16x16x32_f16 v[144:147], v[40:43], v[112:115], 0
	v_mfma_f32_16x16x32_f16 v[148:151], v[44:47], v[112:115], 0
	v_min3_i32 v160, v120, v121, s41
	v_min3_i32 v160, v122, v123, v160
	v_min3_i32 v160, v124, v125, v160
	v_min3_i32 v160, v126, v127, v160
	v_min3_i32 v160, v128, v129, v160
	v_min3_i32 v160, v130, v131, v160
	v_min3_i32 v160, v132, v133, v160
	v_min3_i32 v157, v134, v135, v160
	v_mov_b32_e32 v6, 0
	v_mov_b32_e32 v7, 0x900
	v_mov_b32_e32 v8, 0x240
	s_waitcnt vmcnt(17)
	v_mfma_f32_16x16x32_f16 v[120:123], v[48:51], v[112:115], 0
	v_mfma_f32_16x16x32_f16 v[124:127], v[52:55], v[112:115], 0
	v_mov_b32_e32 v158, 0
	v_mfma_f32_16x16x32_f16 v[128:131], v[56:59], v[112:115], 0
	v_mfma_f32_16x16x32_f16 v[132:135], v[60:63], v[112:115], 0
	v_min3_i32 v160, v136, v137, v157
	v_min3_i32 v160, v138, v139, v160
	v_min3_i32 v160, v140, v141, v160
	v_min3_i32 v160, v142, v143, v160
	v_min3_i32 v160, v144, v145, v160
	v_min3_i32 v160, v146, v147, v160
	v_min3_i32 v160, v148, v149, v160
	v_min3_i32 v156, v150, v151, v160
	v_cmp_ge_i32_e32 vcc, v156, v157
	s_waitcnt vmcnt(13)
	v_mfma_f32_16x16x32_f16 v[136:139], v[64:67], v[112:115], 0
	v_mfma_f32_16x16x32_f16 v[140:143], v[68:71], v[112:115], 0
	v_cndmask_b32_e32 v158, 1, v158, vcc
	v_mfma_f32_16x16x32_f16 v[144:147], v[72:75], v[112:115], 0
	v_mfma_f32_16x16x32_f16 v[148:151], v[76:79], v[112:115], 0
	v_min3_i32 v160, v120, v121, v156
	v_min3_i32 v160, v122, v123, v160
	v_min3_i32 v160, v124, v125, v160
	v_min3_i32 v160, v126, v127, v160
	v_min3_i32 v160, v128, v129, v160
	v_min3_i32 v160, v130, v131, v160
	v_min3_i32 v160, v132, v133, v160
	v_min3_i32 v157, v134, v135, v160
	v_cmp_ge_i32_e32 vcc, v157, v156
	s_waitcnt vmcnt(9)
	v_mfma_f32_16x16x32_f16 v[120:123], v[80:83], v[112:115], 0
	v_mfma_f32_16x16x32_f16 v[124:127], v[84:87], v[112:115], 0
	v_cndmask_b32_e32 v158, 2, v158, vcc
	v_mfma_f32_16x16x32_f16 v[128:131], v[88:91], v[112:115], 0
	v_mfma_f32_16x16x32_f16 v[132:135], v[92:95], v[112:115], 0
	v_min3_i32 v160, v136, v137, v157
	v_min3_i32 v160, v138, v139, v160
	v_min3_i32 v160, v140, v141, v160
	v_min3_i32 v160, v142, v143, v160
	v_min3_i32 v160, v144, v145, v160
	v_min3_i32 v160, v146, v147, v160
	v_min3_i32 v160, v148, v149, v160
	v_min3_i32 v156, v150, v151, v160
	v_cmp_ge_i32_e32 vcc, v156, v157
	s_waitcnt vmcnt(5)
	v_mfma_f32_16x16x32_f16 v[136:139], v[96:99], v[112:115], 0
	v_mfma_f32_16x16x32_f16 v[140:143], v[100:103], v[112:115], 0
	v_cndmask_b32_e32 v158, 3, v158, vcc
	v_mfma_f32_16x16x32_f16 v[144:147], v[104:107], v[112:115], 0
	v_mfma_f32_16x16x32_f16 v[148:151], v[108:111], v[112:115], 0
	v_min3_i32 v160, v120, v121, v156
	v_min3_i32 v160, v122, v123, v160
	v_min3_i32 v160, v124, v125, v160
	v_min3_i32 v160, v126, v127, v160
	v_min3_i32 v160, v128, v129, v160
	v_min3_i32 v160, v130, v131, v160
	v_min3_i32 v160, v132, v133, v160
	v_min3_i32 v157, v134, v135, v160
	v_cmp_ge_i32_e32 vcc, v157, v156
	s_waitcnt vmcnt(4)
	global_load_dwordx4 v[112:115], v164, s[4:5] offset:2048
	v_mfma_f32_16x16x32_f16 v[120:123], v[16:19], v[116:119], 0
	v_mfma_f32_16x16x32_f16 v[124:127], v[20:23], v[116:119], 0
	v_cndmask_b32_e32 v158, 4, v158, vcc
	v_mfma_f32_16x16x32_f16 v[128:131], v[24:27], v[116:119], 0
	v_mfma_f32_16x16x32_f16 v[132:135], v[28:31], v[116:119], 0
	v_min3_i32 v160, v136, v137, v157
	v_min3_i32 v160, v138, v139, v160
	v_min3_i32 v160, v140, v141, v160
	v_min3_i32 v160, v142, v143, v160
	v_min3_i32 v160, v144, v145, v160
	v_min3_i32 v160, v146, v147, v160
	v_min3_i32 v160, v148, v149, v160
	v_min3_i32 v156, v150, v151, v160
	v_cmp_ge_i32_e32 vcc, v156, v157
	v_mfma_f32_16x16x32_f16 v[136:139], v[32:35], v[116:119], 0
	v_mfma_f32_16x16x32_f16 v[140:143], v[36:39], v[116:119], 0
	v_cndmask_b32_e32 v158, 5, v158, vcc
	v_add_u32_e32 v162, s40, v158
	v_lshl_or_b32 v162, v162, 2, v166
	v_mov_b32_e32 v163, v156
	ds_min_u64 v167, v[162:163] offset:16384
	v_mfma_f32_16x16x32_f16 v[144:147], v[40:43], v[116:119], 0
	v_mfma_f32_16x16x32_f16 v[148:151], v[44:47], v[116:119], 0
	v_min3_i32 v160, v120, v121, s41
	v_min3_i32 v160, v122, v123, v160
	v_min3_i32 v160, v124, v125, v160
	v_min3_i32 v160, v126, v127, v160
	v_min3_i32 v160, v128, v129, v160
	v_min3_i32 v160, v130, v131, v160
	v_min3_i32 v160, v132, v133, v160
	v_min3_i32 v157, v134, v135, v160
	v_mfma_f32_16x16x32_f16 v[120:123], v[48:51], v[116:119], 0
	v_mfma_f32_16x16x32_f16 v[124:127], v[52:55], v[116:119], 0
	v_mov_b32_e32 v158, 0
	v_mfma_f32_16x16x32_f16 v[128:131], v[56:59], v[116:119], 0
	v_mfma_f32_16x16x32_f16 v[132:135], v[60:63], v[116:119], 0
	v_min3_i32 v160, v136, v137, v157
	v_min3_i32 v160, v138, v139, v160
	v_min3_i32 v160, v140, v141, v160
	v_min3_i32 v160, v142, v143, v160
	v_min3_i32 v160, v144, v145, v160
	v_min3_i32 v160, v146, v147, v160
	v_min3_i32 v160, v148, v149, v160
	v_min3_i32 v156, v150, v151, v160
	v_cmp_ge_i32_e32 vcc, v156, v157
	v_mfma_f32_16x16x32_f16 v[136:139], v[64:67], v[116:119], 0
	v_mfma_f32_16x16x32_f16 v[140:143], v[68:71], v[116:119], 0
	v_cndmask_b32_e32 v158, 1, v158, vcc
	v_mfma_f32_16x16x32_f16 v[144:147], v[72:75], v[116:119], 0
	v_mfma_f32_16x16x32_f16 v[148:151], v[76:79], v[116:119], 0
	v_min3_i32 v160, v120, v121, v156
	v_min3_i32 v160, v122, v123, v160
	v_min3_i32 v160, v124, v125, v160
	v_min3_i32 v160, v126, v127, v160
	v_min3_i32 v160, v128, v129, v160
	v_min3_i32 v160, v130, v131, v160
	v_min3_i32 v160, v132, v133, v160
	v_min3_i32 v157, v134, v135, v160
	v_cmp_ge_i32_e32 vcc, v157, v156
	v_mfma_f32_16x16x32_f16 v[120:123], v[80:83], v[116:119], 0
	v_mfma_f32_16x16x32_f16 v[124:127], v[84:87], v[116:119], 0
	v_cndmask_b32_e32 v158, 2, v158, vcc
	v_mfma_f32_16x16x32_f16 v[128:131], v[88:91], v[116:119], 0
	v_mfma_f32_16x16x32_f16 v[132:135], v[92:95], v[116:119], 0
	v_min3_i32 v160, v136, v137, v157
	v_min3_i32 v160, v138, v139, v160
	v_min3_i32 v160, v140, v141, v160
	v_min3_i32 v160, v142, v143, v160
	v_min3_i32 v160, v144, v145, v160
	v_min3_i32 v160, v146, v147, v160
	v_min3_i32 v160, v148, v149, v160
	v_min3_i32 v156, v150, v151, v160
	v_cmp_ge_i32_e32 vcc, v156, v157
	v_mfma_f32_16x16x32_f16 v[136:139], v[96:99], v[116:119], 0
	v_mfma_f32_16x16x32_f16 v[140:143], v[100:103], v[116:119], 0
	v_cndmask_b32_e32 v158, 3, v158, vcc
	v_mfma_f32_16x16x32_f16 v[144:147], v[104:107], v[116:119], 0
	v_mfma_f32_16x16x32_f16 v[148:151], v[108:111], v[116:119], 0
	v_min3_i32 v160, v120, v121, v156
	v_min3_i32 v160, v122, v123, v160
	v_min3_i32 v160, v124, v125, v160
	v_min3_i32 v160, v126, v127, v160
	v_min3_i32 v160, v128, v129, v160
	v_min3_i32 v160, v130, v131, v160
	v_min3_i32 v160, v132, v133, v160
	v_min3_i32 v157, v134, v135, v160
	v_cmp_ge_i32_e32 vcc, v157, v156
	s_waitcnt vmcnt(0)
	global_load_dwordx4 v[116:119], v164, s[4:5] offset:3072
	v_mfma_f32_16x16x32_f16 v[120:123], v[16:19], v[112:115], 0
	v_mfma_f32_16x16x32_f16 v[124:127], v[20:23], v[112:115], 0
	v_cndmask_b32_e32 v158, 4, v158, vcc
	v_mfma_f32_16x16x32_f16 v[128:131], v[24:27], v[112:115], 0
	v_mfma_f32_16x16x32_f16 v[132:135], v[28:31], v[112:115], 0
	v_min3_i32 v160, v136, v137, v157
	v_min3_i32 v160, v138, v139, v160
	v_min3_i32 v160, v140, v141, v160
	v_min3_i32 v160, v142, v143, v160
	v_min3_i32 v160, v144, v145, v160
	v_min3_i32 v160, v146, v147, v160
	v_min3_i32 v160, v148, v149, v160
	v_min3_i32 v156, v150, v151, v160
	v_cmp_ge_i32_e32 vcc, v156, v157
	v_mfma_f32_16x16x32_f16 v[136:139], v[32:35], v[112:115], 0
	v_mfma_f32_16x16x32_f16 v[140:143], v[36:39], v[112:115], 0
	v_cndmask_b32_e32 v158, 5, v158, vcc
	v_add_u32_e32 v162, s40, v158
	v_lshl_or_b32 v162, v162, 2, v166
	v_mov_b32_e32 v163, v156
	ds_min_u64 v167, v[162:163] offset:16512
	v_mfma_f32_16x16x32_f16 v[144:147], v[40:43], v[112:115], 0
	v_mfma_f32_16x16x32_f16 v[148:151], v[44:47], v[112:115], 0
	v_min3_i32 v160, v120, v121, s41
	v_min3_i32 v160, v122, v123, v160
	v_min3_i32 v160, v124, v125, v160
	v_min3_i32 v160, v126, v127, v160
	v_min3_i32 v160, v128, v129, v160
	v_min3_i32 v160, v130, v131, v160
	v_min3_i32 v160, v132, v133, v160
	v_min3_i32 v157, v134, v135, v160
	v_mfma_f32_16x16x32_f16 v[120:123], v[48:51], v[112:115], 0
	v_mfma_f32_16x16x32_f16 v[124:127], v[52:55], v[112:115], 0
	v_mov_b32_e32 v158, 0
	v_mfma_f32_16x16x32_f16 v[128:131], v[56:59], v[112:115], 0
	v_mfma_f32_16x16x32_f16 v[132:135], v[60:63], v[112:115], 0
	v_min3_i32 v160, v136, v137, v157
	v_min3_i32 v160, v138, v139, v160
	v_min3_i32 v160, v140, v141, v160
	v_min3_i32 v160, v142, v143, v160
	v_min3_i32 v160, v144, v145, v160
	v_min3_i32 v160, v146, v147, v160
	v_min3_i32 v160, v148, v149, v160
	v_min3_i32 v156, v150, v151, v160
	v_cmp_ge_i32_e32 vcc, v156, v157
	v_mfma_f32_16x16x32_f16 v[136:139], v[64:67], v[112:115], 0
	v_mfma_f32_16x16x32_f16 v[140:143], v[68:71], v[112:115], 0
	v_cndmask_b32_e32 v158, 1, v158, vcc
	v_mfma_f32_16x16x32_f16 v[144:147], v[72:75], v[112:115], 0
	v_mfma_f32_16x16x32_f16 v[148:151], v[76:79], v[112:115], 0
	v_min3_i32 v160, v120, v121, v156
	v_min3_i32 v160, v122, v123, v160
	v_min3_i32 v160, v124, v125, v160
	v_min3_i32 v160, v126, v127, v160
	v_min3_i32 v160, v128, v129, v160
	v_min3_i32 v160, v130, v131, v160
	v_min3_i32 v160, v132, v133, v160
	v_min3_i32 v157, v134, v135, v160
	v_cmp_ge_i32_e32 vcc, v157, v156
	v_mfma_f32_16x16x32_f16 v[120:123], v[80:83], v[112:115], 0
	v_mfma_f32_16x16x32_f16 v[124:127], v[84:87], v[112:115], 0
	v_cndmask_b32_e32 v158, 2, v158, vcc
	v_mfma_f32_16x16x32_f16 v[128:131], v[88:91], v[112:115], 0
	v_mfma_f32_16x16x32_f16 v[132:135], v[92:95], v[112:115], 0
	v_min3_i32 v160, v136, v137, v157
	v_min3_i32 v160, v138, v139, v160
	v_min3_i32 v160, v140, v141, v160
	v_min3_i32 v160, v142, v143, v160
	v_min3_i32 v160, v144, v145, v160
	v_min3_i32 v160, v146, v147, v160
	v_min3_i32 v160, v148, v149, v160
	v_min3_i32 v156, v150, v151, v160
	v_cmp_ge_i32_e32 vcc, v156, v157
	v_mfma_f32_16x16x32_f16 v[136:139], v[96:99], v[112:115], 0
	v_mfma_f32_16x16x32_f16 v[140:143], v[100:103], v[112:115], 0
	v_cndmask_b32_e32 v158, 3, v158, vcc
	v_mfma_f32_16x16x32_f16 v[144:147], v[104:107], v[112:115], 0
	v_mfma_f32_16x16x32_f16 v[148:151], v[108:111], v[112:115], 0
	v_min3_i32 v160, v120, v121, v156
	v_min3_i32 v160, v122, v123, v160
	v_min3_i32 v160, v124, v125, v160
	v_min3_i32 v160, v126, v127, v160
	v_min3_i32 v160, v128, v129, v160
	v_min3_i32 v160, v130, v131, v160
	v_min3_i32 v160, v132, v133, v160
	v_min3_i32 v157, v134, v135, v160
	v_cmp_ge_i32_e32 vcc, v157, v156
	s_waitcnt vmcnt(0)
	global_load_dwordx4 v[112:115], v164, s[22:23]
	v_mfma_f32_16x16x32_f16 v[120:123], v[16:19], v[116:119], 0
	v_mfma_f32_16x16x32_f16 v[124:127], v[20:23], v[116:119], 0
	v_cndmask_b32_e32 v158, 4, v158, vcc
	v_mfma_f32_16x16x32_f16 v[128:131], v[24:27], v[116:119], 0
	v_mfma_f32_16x16x32_f16 v[132:135], v[28:31], v[116:119], 0
	v_min3_i32 v160, v136, v137, v157
	v_min3_i32 v160, v138, v139, v160
	v_min3_i32 v160, v140, v141, v160
	v_min3_i32 v160, v142, v143, v160
	v_min3_i32 v160, v144, v145, v160
	v_min3_i32 v160, v146, v147, v160
	v_min3_i32 v160, v148, v149, v160
	v_min3_i32 v156, v150, v151, v160
	v_cmp_ge_i32_e32 vcc, v156, v157
	v_mfma_f32_16x16x32_f16 v[136:139], v[32:35], v[116:119], 0
	v_mfma_f32_16x16x32_f16 v[140:143], v[36:39], v[116:119], 0
	v_cndmask_b32_e32 v158, 5, v158, vcc
	v_add_u32_e32 v162, s40, v158
	v_lshl_or_b32 v162, v162, 2, v166
	v_mov_b32_e32 v163, v156
	ds_min_u64 v167, v[162:163] offset:16640
	v_mfma_f32_16x16x32_f16 v[144:147], v[40:43], v[116:119], 0
	v_mfma_f32_16x16x32_f16 v[148:151], v[44:47], v[116:119], 0
	v_min3_i32 v160, v120, v121, s41
	v_min3_i32 v160, v122, v123, v160
	v_min3_i32 v160, v124, v125, v160
	v_min3_i32 v160, v126, v127, v160
	v_min3_i32 v160, v128, v129, v160
	v_min3_i32 v160, v130, v131, v160
	v_min3_i32 v160, v132, v133, v160
	v_min3_i32 v157, v134, v135, v160
	s_waitcnt lgkmcnt(0)
	s_barrier
	s_cmp_lt_u32 s50, 3
	s_cbranch_scc0 .Lp1a_3_x
	s_lshl_b32 s60, s50, 7
	v_add_u32_e32 v2, s60, v169
	ds_read_b32 v178, v2 offset:16384
	s_lshl_b32 s60, s50, 10
	v_add_u32_e32 v210, s60, v170

.Lit4b:
	global_load_dwordx4 v[116:119], v164, s[22:23] offset:1024
	v_mfma_f32_16x16x32_f16 v[120:123], v[16:19], v[112:115], 0
	v_mfma_f32_16x16x32_f16 v[124:127], v[20:23], v[112:115], 0
	v_cndmask_b32_e32 v158, 4, v158, vcc
	v_mfma_f32_16x16x32_f16 v[128:131], v[24:27], v[112:115], 0
	v_mfma_f32_16x16x32_f16 v[132:135], v[28:31], v[112:115], 0
	v_min3_i32 v160, v136, v137, v157
	v_min3_i32 v160, v138, v139, v160
	v_min3_i32 v160, v140, v141, v160
	v_min3_i32 v160, v142, v143, v160
	v_min3_i32 v160, v144, v145, v160
	v_min3_i32 v160, v146, v147, v160
	v_min3_i32 v160, v148, v149, v160
	v_min3_i32 v156, v150, v151, v160
	v_cmp_ge_i32_e32 vcc, v156, v157
	v_mfma_f32_16x16x32_f16 v[136:139], v[32:35], v[112:115], 0
	v_mfma_f32_16x16x32_f16 v[140:143], v[36:39], v[112:115], 0
	v_cndmask_b32_e32 v158, 5, v158, vcc
	v_add_u32_e32 v162, s40, v158
	v_lshl_or_b32 v162, v162, 2, v166
	v_mov_b32_e32 v163, v156
	ds_min_u64 v167, v[162:163] offset:16768
	v_mfma_f32_16x16x32_f16 v[144:147], v[40:43], v[112:115], 0
	v_mfma_f32_16x16x32_f16 v[148:151], v[44:47], v[112:115], 0
	v_min3_i32 v160, v120, v121, s41
	v_min3_i32 v160, v122, v123, v160
	v_min3_i32 v160, v124, v125, v160
	v_min3_i32 v160, v126, v127, v160
	v_min3_i32 v160, v128, v129, v160
	v_min3_i32 v160, v130, v131, v160
	v_min3_i32 v160, v132, v133, v160
	v_min3_i32 v157, v134, v135, v160
	v_mfma_f32_16x16x32_f16 v[120:123], v[48:51], v[112:115], 0
	v_mfma_f32_16x16x32_f16 v[124:127], v[52:55], v[112:115], 0
	v_mov_b32_e32 v158, 0
	v_mfma_f32_16x16x32_f16 v[128:131], v[56:59], v[112:115], 0
	v_mfma_f32_16x16x32_f16 v[132:135], v[60:63], v[112:115], 0
	v_min3_i32 v160, v136, v137, v157
	v_min3_i32 v160, v138, v139, v160
	v_min3_i32 v160, v140, v141, v160
	v_min3_i32 v160, v142, v143, v160
	v_min3_i32 v160, v144, v145, v160
	v_min3_i32 v160, v146, v147, v160
	v_min3_i32 v160, v148, v149, v160
	v_min3_i32 v156, v150, v151, v160
	v_cmp_ge_i32_e32 vcc, v156, v157
	v_mfma_f32_16x16x32_f16 v[136:139], v[64:67], v[112:115], 0
	v_mfma_f32_16x16x32_f16 v[140:143], v[68:71], v[112:115], 0
	v_cndmask_b32_e32 v158, 1, v158, vcc
	v_mfma_f32_16x16x32_f16 v[144:147], v[72:75], v[112:115], 0
	v_mfma_f32_16x16x32_f16 v[148:151], v[76:79], v[112:115], 0
	v_min3_i32 v160, v120, v121, v156
	v_min3_i32 v160, v122, v123, v160
	v_min3_i32 v160, v124, v125, v160
	v_min3_i32 v160, v126, v127, v160
	v_min3_i32 v160, v128, v129, v160
	v_min3_i32 v160, v130, v131, v160
	v_min3_i32 v160, v132, v133, v160
	v_min3_i32 v157, v134, v135, v160
	v_cmp_ge_i32_e32 vcc, v157, v156
	v_mfma_f32_16x16x32_f16 v[120:123], v[80:83], v[112:115], 0
	v_mfma_f32_16x16x32_f16 v[124:127], v[84:87], v[112:115], 0
	v_cndmask_b32_e32 v158, 2, v158, vcc
	v_mfma_f32_16x16x32_f16 v[128:131], v[88:91], v[112:115], 0
	v_mfma_f32_16x16x32_f16 v[132:135], v[92:95], v[112:115], 0
	v_min3_i32 v160, v136, v137, v157
	v_min3_i32 v160, v138, v139, v160
	v_min3_i32 v160, v140, v141, v160
	v_min3_i32 v160, v142, v143, v160
	v_min3_i32 v160, v144, v145, v160
	v_min3_i32 v160, v146, v147, v160
	v_min3_i32 v160, v148, v149, v160
	v_min3_i32 v156, v150, v151, v160
	v_cmp_ge_i32_e32 vcc, v156, v157
	v_mfma_f32_16x16x32_f16 v[136:139], v[96:99], v[112:115], 0
	v_mfma_f32_16x16x32_f16 v[140:143], v[100:103], v[112:115], 0
	v_cndmask_b32_e32 v158, 3, v158, vcc
	v_mfma_f32_16x16x32_f16 v[144:147], v[104:107], v[112:115], 0
	v_mfma_f32_16x16x32_f16 v[148:151], v[108:111], v[112:115], 0
	v_min3_i32 v160, v120, v121, v156
	v_min3_i32 v160, v122, v123, v160
	v_min3_i32 v160, v124, v125, v160
	v_min3_i32 v160, v126, v127, v160
	v_min3_i32 v160, v128, v129, v160
	v_min3_i32 v160, v130, v131, v160
	v_min3_i32 v160, v132, v133, v160
	v_min3_i32 v157, v134, v135, v160
	v_cmp_ge_i32_e32 vcc, v157, v156
	s_waitcnt vmcnt(0)
	global_load_dwordx4 v[112:115], v164, s[22:23] offset:2048
	v_mfma_f32_16x16x32_f16 v[120:123], v[16:19], v[116:119], 0
	v_mfma_f32_16x16x32_f16 v[124:127], v[20:23], v[116:119], 0
	v_cndmask_b32_e32 v158, 4, v158, vcc
	v_mfma_f32_16x16x32_f16 v[128:131], v[24:27], v[116:119], 0
	v_mfma_f32_16x16x32_f16 v[132:135], v[28:31], v[116:119], 0
	v_min3_i32 v160, v136, v137, v157
	v_min3_i32 v160, v138, v139, v160
	v_min3_i32 v160, v140, v141, v160
	v_min3_i32 v160, v142, v143, v160
	v_min3_i32 v160, v144, v145, v160
	v_min3_i32 v160, v146, v147, v160
	v_min3_i32 v160, v148, v149, v160
	v_min3_i32 v156, v150, v151, v160
	v_cmp_ge_i32_e32 vcc, v156, v157
	v_mfma_f32_16x16x32_f16 v[136:139], v[32:35], v[116:119], 0
	v_mfma_f32_16x16x32_f16 v[140:143], v[36:39], v[116:119], 0
	v_cndmask_b32_e32 v158, 5, v158, vcc
	v_add_u32_e32 v162, s40, v158
	v_lshl_or_b32 v162, v162, 2, v166
	v_mov_b32_e32 v163, v156
	ds_min_u64 v167, v[162:163] offset:16896
	v_mfma_f32_16x16x32_f16 v[144:147], v[40:43], v[116:119], 0
	v_mfma_f32_16x16x32_f16 v[148:151], v[44:47], v[116:119], 0
	v_min3_i32 v160, v120, v121, s41
	v_min3_i32 v160, v122, v123, v160
	v_min3_i32 v160, v124, v125, v160
	v_min3_i32 v160, v126, v127, v160
	v_min3_i32 v160, v128, v129, v160
	v_min3_i32 v160, v130, v131, v160
	v_min3_i32 v160, v132, v133, v160
	v_min3_i32 v157, v134, v135, v160
	v_mfma_f32_16x16x32_f16 v[120:123], v[48:51], v[116:119], 0
	v_mfma_f32_16x16x32_f16 v[124:127], v[52:55], v[116:119], 0
	v_mov_b32_e32 v158, 0
	v_mfma_f32_16x16x32_f16 v[128:131], v[56:59], v[116:119], 0
	v_mfma_f32_16x16x32_f16 v[132:135], v[60:63], v[116:119], 0
	v_min3_i32 v160, v136, v137, v157
	v_min3_i32 v160, v138, v139, v160
	v_min3_i32 v160, v140, v141, v160
	v_min3_i32 v160, v142, v143, v160
	v_min3_i32 v160, v144, v145, v160
	v_min3_i32 v160, v146, v147, v160
	v_min3_i32 v160, v148, v149, v160
	v_min3_i32 v156, v150, v151, v160
	v_cmp_ge_i32_e32 vcc, v156, v157
	v_mfma_f32_16x16x32_f16 v[136:139], v[64:67], v[116:119], 0
	v_mfma_f32_16x16x32_f16 v[140:143], v[68:71], v[116:119], 0
	v_cndmask_b32_e32 v158, 1, v158, vcc
	v_mfma_f32_16x16x32_f16 v[144:147], v[72:75], v[116:119], 0
	v_mfma_f32_16x16x32_f16 v[148:151], v[76:79], v[116:119], 0
	v_min3_i32 v160, v120, v121, v156
	v_min3_i32 v160, v122, v123, v160
	v_min3_i32 v160, v124, v125, v160
	v_min3_i32 v160, v126, v127, v160
	v_min3_i32 v160, v128, v129, v160
	v_min3_i32 v160, v130, v131, v160
	v_min3_i32 v160, v132, v133, v160
	v_min3_i32 v157, v134, v135, v160
	v_cmp_ge_i32_e32 vcc, v157, v156
	v_mfma_f32_16x16x32_f16 v[120:123], v[80:83], v[116:119], 0
	v_mfma_f32_16x16x32_f16 v[124:127], v[84:87], v[116:119], 0
	v_cndmask_b32_e32 v158, 2, v158, vcc
	v_mfma_f32_16x16x32_f16 v[128:131], v[88:91], v[116:119], 0
	v_mfma_f32_16x16x32_f16 v[132:135], v[92:95], v[116:119], 0
	v_min3_i32 v160, v136, v137, v157
	v_min3_i32 v160, v138, v139, v160
	v_min3_i32 v160, v140, v141, v160
	v_min3_i32 v160, v142, v143, v160
	v_min3_i32 v160, v144, v145, v160
	v_min3_i32 v160, v146, v147, v160
	v_min3_i32 v160, v148, v149, v160
	v_min3_i32 v156, v150, v151, v160
	v_cmp_ge_i32_e32 vcc, v156, v157
	v_mfma_f32_16x16x32_f16 v[136:139], v[96:99], v[116:119], 0
	v_mfma_f32_16x16x32_f16 v[140:143], v[100:103], v[116:119], 0
	v_cndmask_b32_e32 v158, 3, v158, vcc
	v_mfma_f32_16x16x32_f16 v[144:147], v[104:107], v[116:119], 0
	v_mfma_f32_16x16x32_f16 v[148:151], v[108:111], v[116:119], 0
	v_min3_i32 v160, v120, v121, v156
	v_min3_i32 v160, v122, v123, v160
	v_min3_i32 v160, v124, v125, v160
	v_min3_i32 v160, v126, v127, v160
	v_min3_i32 v160, v128, v129, v160
	v_min3_i32 v160, v130, v131, v160
	v_min3_i32 v160, v132, v133, v160
	v_min3_i32 v157, v134, v135, v160
	v_cmp_ge_i32_e32 vcc, v157, v156
	s_waitcnt vmcnt(0)
	global_load_dwordx4 v[116:119], v164, s[22:23] offset:3072
	v_mfma_f32_16x16x32_f16 v[120:123], v[16:19], v[112:115], 0
	v_mfma_f32_16x16x32_f16 v[124:127], v[20:23], v[112:115], 0
	v_cndmask_b32_e32 v158, 4, v158, vcc
	v_mfma_f32_16x16x32_f16 v[128:131], v[24:27], v[112:115], 0
	v_mfma_f32_16x16x32_f16 v[132:135], v[28:31], v[112:115], 0
	v_min3_i32 v160, v136, v137, v157
	v_min3_i32 v160, v138, v139, v160
	v_min3_i32 v160, v140, v141, v160
	v_min3_i32 v160, v142, v143, v160
	v_min3_i32 v160, v144, v145, v160
	v_min3_i32 v160, v146, v147, v160
	v_min3_i32 v160, v148, v149, v160
	v_min3_i32 v156, v150, v151, v160
	v_cmp_ge_i32_e32 vcc, v156, v157
	v_mfma_f32_16x16x32_f16 v[136:139], v[32:35], v[112:115], 0
	v_mfma_f32_16x16x32_f16 v[140:143], v[36:39], v[112:115], 0
	v_cndmask_b32_e32 v158, 5, v158, vcc
	v_add_u32_e32 v162, s40, v158
	v_lshl_or_b32 v162, v162, 2, v166
	v_mov_b32_e32 v163, v156
	ds_min_u64 v167, v[162:163] offset:17024
	v_mfma_f32_16x16x32_f16 v[144:147], v[40:43], v[112:115], 0
	v_mfma_f32_16x16x32_f16 v[148:151], v[44:47], v[112:115], 0
	v_min3_i32 v160, v120, v121, s41
	v_min3_i32 v160, v122, v123, v160
	v_min3_i32 v160, v124, v125, v160
	v_min3_i32 v160, v126, v127, v160
	v_min3_i32 v160, v128, v129, v160
	v_min3_i32 v160, v130, v131, v160
	v_min3_i32 v160, v132, v133, v160
	v_min3_i32 v157, v134, v135, v160
	s_waitcnt lgkmcnt(0)
	s_barrier
	s_cmp_eq_u32 s50, 3
	s_cbranch_scc0 .Lp1a_6_x
	s_lshl_b32 s60, s50, 7
	v_add_u32_e32 v2, s60, v169
	ds_read_b32 v178, v2 offset:16384
	s_lshl_b32 s60, s50, 10
	v_add_u32_e32 v210, s60, v170

.Lq6:
	s_nop 1
	v_add_f32_dpp v6, v6, v6 quad_perm:[1,0,3,2] row_mask:0xf bank_mask:0xf
	s_nop 1
	v_add_f32_dpp v6, v6, v6 quad_perm:[2,3,0,1] row_mask:0xf bank_mask:0xf
	s_nop 1
	v_add_f32_dpp v6, v6, v6 row_half_mirror row_mask:0xf bank_mask:0xf
	s_nop 1
	v_add_f32_dpp v6, v6, v6 row_mirror row_mask:0xf bank_mask:0xf
	s_nop 1
	v_add_f32_dpp v6, v6, v6 row_bcast:15 row_mask:0xa bank_mask:0xf
	s_nop 1
	v_add_f32_dpp v6, v6, v6 row_bcast:31 row_mask:0xc bank_mask:0xf
	s_lshl_b32 s60, s15, 2
	v_mov_b32_e32 v2, s60
	s_mov_b64 s[52:53], exec
	s_mov_b32 exec_lo, 0
	s_mov_b32 exec_hi, 0x80000000
	ds_write_b32 v2, v6 offset:18112
	s_mov_b64 exec, s[52:53]
	v_cmp_eq_u32_e32 vcc, 0, v0
	s_waitcnt lgkmcnt(0)
	s_barrier
	s_and_saveexec_b64 s[0:1], vcc
	s_cbranch_execz .LBB1_34
	v_mov_b32_e32 v0, 0
	ds_read_b128 v[2:5], v0 offset:18112
	ds_read_b128 v[6:9], v0 offset:18128
	s_mov_b64 s[6:7], exec
	s_waitcnt lgkmcnt(0)
	v_add_f32_e32 v1, v2, v3
	v_add_f32_e32 v1, v1, v4
	v_add_f32_e32 v1, v1, v5
	v_add_f32_e32 v1, v1, v6
	v_add_f32_e32 v1, v1, v7
	v_add_f32_e32 v1, v1, v8
	v_add_f32_e32 v1, v1, v9
	v_mul_f32_e32 v1, 0x49800000, v1
	v_cvt_u32_f32_e32 v2, v1
	v_mbcnt_lo_u32_b32 v1, s6, 0
	v_mbcnt_hi_u32_b32 v1, s7, v1
	v_cmp_eq_u32_e32 vcc, 0, v1
	s_and_saveexec_b64 s[0:1], vcc
	s_cbranch_execz .LBB1_27
	s_lshl_b32 s8, s14, 4
	s_ashr_i32 s9, s8, 31
	s_lshl_b64 s[8:9], s[8:9], 3
	s_add_u32 s8, s4, s8
	s_addc_u32 s9, s5, s9
	s_bcnt1_i32_b64 s6, s[6:7]
	v_mov_b32_e32 v3, 0x1000000
	v_mul_lo_u32 v3, v3, s6
	v_mul_hi_u32 v4, v2, s6
	v_add_u32_e32 v5, v4, v3
	v_mul_lo_u32 v4, v2, s6
	v_mov_b32_e32 v3, 0x663000
	global_atomic_add_x2 v[4:5], v3, v[4:5], s[8:9] offset:3072 sc0
